# split-K tail exchange read-back (proj, gate|up): 16 loads per partner part issued in one batch, single wait, instead of load/wait ladder
# baseline (speedup 1.0000x reference)
.LBB0_1024:
	s_or_b32 s6, s6, s27
	s_ashr_i32 s7, s6, 31
	s_lshl_b64 s[42:43], s[6:7], 17
	v_lshl_add_u64 v[158:159], v[142:143], 0, s[42:43]
	global_load_dwordx4 v[184:187], v[158:159], off
	global_load_dwordx4 v[188:191], v[158:159], off offset:1024
	v_add_co_u32_e32 v248, vcc, 0x4000, v158
	s_nop 1
	v_addc_co_u32_e32 v249, vcc, 0, v159, vcc
	global_load_dwordx4 v[192:195], v[248:249], off
	global_load_dwordx4 v[196:199], v[248:249], off offset:1024
	v_add_co_u32_e32 v248, vcc, 0x8000, v158
	s_nop 1
	v_addc_co_u32_e32 v249, vcc, 0, v159, vcc
	global_load_dwordx4 v[200:203], v[248:249], off
	global_load_dwordx4 v[204:207], v[248:249], off offset:1024
	v_add_co_u32_e32 v248, vcc, 0xc000, v158
	s_nop 1
	v_addc_co_u32_e32 v249, vcc, 0, v159, vcc
	global_load_dwordx4 v[208:211], v[248:249], off
	global_load_dwordx4 v[212:215], v[248:249], off offset:1024
	v_add_co_u32_e32 v248, vcc, 0x10000, v158
	s_nop 1
	v_addc_co_u32_e32 v249, vcc, 0, v159, vcc
	global_load_dwordx4 v[216:219], v[248:249], off
	global_load_dwordx4 v[220:223], v[248:249], off offset:1024
	v_add_co_u32_e32 v248, vcc, 0x14000, v158
	s_nop 1
	v_addc_co_u32_e32 v249, vcc, 0, v159, vcc
	global_load_dwordx4 v[224:227], v[248:249], off
	global_load_dwordx4 v[228:231], v[248:249], off offset:1024
	v_add_co_u32_e32 v248, vcc, 0x18000, v158
	s_nop 1
	v_addc_co_u32_e32 v249, vcc, 0, v159, vcc
	global_load_dwordx4 v[232:235], v[248:249], off
	global_load_dwordx4 v[236:239], v[248:249], off offset:1024
	v_add_co_u32_e32 v248, vcc, 0x1c000, v158
	s_nop 1
	v_addc_co_u32_e32 v249, vcc, 0, v159, vcc
	global_load_dwordx4 v[240:243], v[248:249], off
	global_load_dwordx4 v[244:247], v[248:249], off offset:1024
	v_cndmask_b32_e64 v138, 0, 1, s[36:37]
	v_cmp_ne_u32_e64 s[6:7], 1, v138
	s_andn2_b64 vcc, exec, s[36:37]
	v_lshl_add_u64 v[158:159], v[142:143], 0, s[42:43]
	s_cbranch_vccz .LBB0_1032
	s_and_b64 vcc, exec, s[6:7]
	s_cbranch_vccz .LBB0_1033

.LBB0_1029:
	s_waitcnt vmcnt(0)
	v_lshlrev_b32_e32 v178, 16, v216
	v_and_b32_e32 v179, 0xffff0000, v216
	v_lshlrev_b32_e32 v216, 16, v217
	v_and_b32_e32 v217, 0xffff0000, v217
	v_lshlrev_b32_e32 v180, 16, v218
	v_and_b32_e32 v181, 0xffff0000, v218
	v_lshlrev_b32_e32 v218, 16, v219
	v_and_b32_e32 v219, 0xffff0000, v219
	v_pk_add_f32 v[62:63], v[62:63], v[216:217]
	v_pk_add_f32 v[54:55], v[54:55], v[218:219]
	v_pk_add_f32 v[60:61], v[60:61], v[178:179]
	v_pk_add_f32 v[52:53], v[52:53], v[180:181]
	s_waitcnt vmcnt(0)
	v_lshlrev_b32_e32 v176, 16, v220
	v_and_b32_e32 v177, 0xffff0000, v220
	v_lshlrev_b32_e32 v220, 16, v221
	v_and_b32_e32 v221, 0xffff0000, v221
	v_lshlrev_b32_e32 v178, 16, v222
	v_and_b32_e32 v179, 0xffff0000, v222
	v_lshlrev_b32_e32 v222, 16, v223
	v_and_b32_e32 v223, 0xffff0000, v223
	v_pk_add_f32 v[58:59], v[58:59], v[220:221]
	v_pk_add_f32 v[56:57], v[56:57], v[176:177]
	v_pk_add_f32 v[50:51], v[50:51], v[222:223]
	v_pk_add_f32 v[48:49], v[48:49], v[178:179]
	s_and_b64 vcc, exec, s[6:7]
	s_cbranch_vccz .LBB0_1037

.LBB0_1031:
	s_waitcnt vmcnt(0)
	v_lshlrev_b32_e32 v178, 16, v232
	v_and_b32_e32 v179, 0xffff0000, v232
	v_lshlrev_b32_e32 v232, 16, v233
	v_and_b32_e32 v233, 0xffff0000, v233
	v_lshlrev_b32_e32 v180, 16, v234
	v_and_b32_e32 v181, 0xffff0000, v234
	v_lshlrev_b32_e32 v234, 16, v235
	v_and_b32_e32 v235, 0xffff0000, v235
	v_pk_add_f32 v[30:31], v[30:31], v[232:233]
	v_pk_add_f32 v[22:23], v[22:23], v[234:235]
	v_pk_add_f32 v[28:29], v[28:29], v[178:179]
	v_pk_add_f32 v[20:21], v[20:21], v[180:181]
	s_waitcnt vmcnt(0)
	v_lshlrev_b32_e32 v176, 16, v236
	v_and_b32_e32 v177, 0xffff0000, v236
	v_lshlrev_b32_e32 v236, 16, v237
	v_and_b32_e32 v237, 0xffff0000, v237
	v_lshlrev_b32_e32 v178, 16, v238
	v_and_b32_e32 v179, 0xffff0000, v238
	v_lshlrev_b32_e32 v238, 16, v239
	v_and_b32_e32 v239, 0xffff0000, v239
	v_pk_add_f32 v[26:27], v[26:27], v[236:237]
	v_pk_add_f32 v[24:25], v[24:25], v[176:177]
	v_pk_add_f32 v[18:19], v[18:19], v[238:239]
	v_pk_add_f32 v[16:17], v[16:17], v[178:179]
	s_and_b64 vcc, exec, s[6:7]
	s_cbranch_vccz .LBB0_1039
	s_branch .LBB0_1040
.LBB0_1032:
	s_waitcnt vmcnt(0)
	v_lshlrev_b32_e32 v176, 16, v184
	v_and_b32_e32 v177, 0xffff0000, v184
	v_lshlrev_b32_e32 v184, 16, v185
	v_and_b32_e32 v185, 0xffff0000, v185
	v_lshlrev_b32_e32 v178, 16, v186
	v_and_b32_e32 v179, 0xffff0000, v186
	v_lshlrev_b32_e32 v186, 16, v187
	v_and_b32_e32 v187, 0xffff0000, v187
	v_pk_add_f32 v[126:127], v[126:127], v[184:185]
	v_pk_add_f32 v[118:119], v[118:119], v[186:187]
	v_pk_add_f32 v[124:125], v[124:125], v[176:177]
	v_pk_add_f32 v[116:117], v[116:117], v[178:179]
	s_waitcnt vmcnt(0)
	v_lshlrev_b32_e32 v176, 16, v188
	v_and_b32_e32 v177, 0xffff0000, v188
	v_lshlrev_b32_e32 v188, 16, v189
	v_and_b32_e32 v189, 0xffff0000, v189
	v_lshlrev_b32_e32 v178, 16, v190
	v_and_b32_e32 v179, 0xffff0000, v190
	v_lshlrev_b32_e32 v190, 16, v191
	v_and_b32_e32 v191, 0xffff0000, v191
	v_pk_add_f32 v[122:123], v[122:123], v[188:189]
	v_pk_add_f32 v[120:121], v[120:121], v[176:177]
	v_pk_add_f32 v[114:115], v[114:115], v[190:191]
	v_pk_add_f32 v[112:113], v[112:113], v[178:179]
	s_and_b64 vcc, exec, s[6:7]
	s_cbranch_vccnz .LBB0_1026
.LBB0_1033:
	s_waitcnt vmcnt(0)
	v_lshlrev_b32_e32 v178, 16, v192
	v_and_b32_e32 v179, 0xffff0000, v192
	v_lshlrev_b32_e32 v192, 16, v193
	v_and_b32_e32 v193, 0xffff0000, v193
	v_lshlrev_b32_e32 v180, 16, v194
	v_and_b32_e32 v181, 0xffff0000, v194
	v_lshlrev_b32_e32 v194, 16, v195
	v_and_b32_e32 v195, 0xffff0000, v195
	v_pk_add_f32 v[110:111], v[110:111], v[192:193]
	v_pk_add_f32 v[102:103], v[102:103], v[194:195]
	v_pk_add_f32 v[108:109], v[108:109], v[178:179]
	v_pk_add_f32 v[100:101], v[100:101], v[180:181]
	s_waitcnt vmcnt(0)
	v_lshlrev_b32_e32 v176, 16, v196
	v_and_b32_e32 v177, 0xffff0000, v196
	v_lshlrev_b32_e32 v196, 16, v197
	v_and_b32_e32 v197, 0xffff0000, v197
	v_lshlrev_b32_e32 v178, 16, v198
	v_and_b32_e32 v179, 0xffff0000, v198
	v_lshlrev_b32_e32 v198, 16, v199
	v_and_b32_e32 v199, 0xffff0000, v199
	v_pk_add_f32 v[106:107], v[106:107], v[196:197]
	v_pk_add_f32 v[104:105], v[104:105], v[176:177]
	v_pk_add_f32 v[98:99], v[98:99], v[198:199]
	v_pk_add_f32 v[96:97], v[96:97], v[178:179]
	s_and_b64 vcc, exec, s[6:7]
	s_cbranch_vccnz .LBB0_1027
.LBB0_1034:
	s_waitcnt vmcnt(0)
	v_lshlrev_b32_e32 v178, 16, v200
	v_and_b32_e32 v179, 0xffff0000, v200
	v_lshlrev_b32_e32 v200, 16, v201
	v_and_b32_e32 v201, 0xffff0000, v201
	v_lshlrev_b32_e32 v180, 16, v202
	v_and_b32_e32 v181, 0xffff0000, v202
	v_lshlrev_b32_e32 v202, 16, v203
	v_and_b32_e32 v203, 0xffff0000, v203
	v_pk_add_f32 v[94:95], v[94:95], v[200:201]
	v_pk_add_f32 v[86:87], v[86:87], v[202:203]
	v_pk_add_f32 v[92:93], v[92:93], v[178:179]
	v_pk_add_f32 v[84:85], v[84:85], v[180:181]
	s_waitcnt vmcnt(0)
	v_lshlrev_b32_e32 v176, 16, v204
	v_and_b32_e32 v177, 0xffff0000, v204
	v_lshlrev_b32_e32 v204, 16, v205
	v_and_b32_e32 v205, 0xffff0000, v205
	v_lshlrev_b32_e32 v178, 16, v206
	v_and_b32_e32 v179, 0xffff0000, v206
	v_lshlrev_b32_e32 v206, 16, v207
	v_and_b32_e32 v207, 0xffff0000, v207
	v_pk_add_f32 v[90:91], v[90:91], v[204:205]
	v_pk_add_f32 v[88:89], v[88:89], v[176:177]
	v_pk_add_f32 v[82:83], v[82:83], v[206:207]
	v_pk_add_f32 v[80:81], v[80:81], v[178:179]
	s_and_b64 vcc, exec, s[6:7]
	s_cbranch_vccnz .LBB0_1028
.LBB0_1035:
	s_waitcnt vmcnt(0)
	v_lshlrev_b32_e32 v178, 16, v208
	v_and_b32_e32 v179, 0xffff0000, v208
	v_lshlrev_b32_e32 v208, 16, v209
	v_and_b32_e32 v209, 0xffff0000, v209
	v_lshlrev_b32_e32 v180, 16, v210
	v_and_b32_e32 v181, 0xffff0000, v210
	v_lshlrev_b32_e32 v210, 16, v211
	v_and_b32_e32 v211, 0xffff0000, v211
	v_pk_add_f32 v[78:79], v[78:79], v[208:209]
	v_pk_add_f32 v[70:71], v[70:71], v[210:211]
	v_pk_add_f32 v[76:77], v[76:77], v[178:179]
	v_pk_add_f32 v[68:69], v[68:69], v[180:181]
	s_waitcnt vmcnt(0)
	v_lshlrev_b32_e32 v176, 16, v212
	v_and_b32_e32 v177, 0xffff0000, v212
	v_lshlrev_b32_e32 v212, 16, v213
	v_and_b32_e32 v213, 0xffff0000, v213
	v_lshlrev_b32_e32 v178, 16, v214
	v_and_b32_e32 v179, 0xffff0000, v214
	v_lshlrev_b32_e32 v214, 16, v215
	v_and_b32_e32 v215, 0xffff0000, v215
	v_pk_add_f32 v[74:75], v[74:75], v[212:213]
	v_pk_add_f32 v[72:73], v[72:73], v[176:177]
	v_pk_add_f32 v[66:67], v[66:67], v[214:215]
	v_pk_add_f32 v[64:65], v[64:65], v[178:179]
	v_cndmask_b32_e64 v138, 0, 1, s[38:39]
	v_cmp_ne_u32_e64 s[6:7], 1, v138
	s_andn2_b64 vcc, exec, s[38:39]
	s_cbranch_vccz .LBB0_1029

.LBB0_1037:
	s_waitcnt vmcnt(0)
	v_lshlrev_b32_e32 v178, 16, v224
	v_and_b32_e32 v179, 0xffff0000, v224
	v_lshlrev_b32_e32 v224, 16, v225
	v_and_b32_e32 v225, 0xffff0000, v225
	v_lshlrev_b32_e32 v180, 16, v226
	v_and_b32_e32 v181, 0xffff0000, v226
	v_lshlrev_b32_e32 v226, 16, v227
	v_and_b32_e32 v227, 0xffff0000, v227
	v_pk_add_f32 v[46:47], v[46:47], v[224:225]
	v_pk_add_f32 v[38:39], v[38:39], v[226:227]
	v_pk_add_f32 v[44:45], v[44:45], v[178:179]
	v_pk_add_f32 v[36:37], v[36:37], v[180:181]
	s_waitcnt vmcnt(0)
	v_lshlrev_b32_e32 v176, 16, v228
	v_and_b32_e32 v177, 0xffff0000, v228
	v_lshlrev_b32_e32 v228, 16, v229
	v_and_b32_e32 v229, 0xffff0000, v229
	v_lshlrev_b32_e32 v178, 16, v230
	v_and_b32_e32 v179, 0xffff0000, v230
	v_lshlrev_b32_e32 v230, 16, v231
	v_and_b32_e32 v231, 0xffff0000, v231
	v_pk_add_f32 v[42:43], v[42:43], v[228:229]
	v_pk_add_f32 v[40:41], v[40:41], v[176:177]
	v_pk_add_f32 v[34:35], v[34:35], v[230:231]
	v_pk_add_f32 v[32:33], v[32:33], v[178:179]
	s_and_b64 vcc, exec, s[6:7]
	s_cbranch_vccz .LBB0_1031

.LBB0_1039:
	s_waitcnt vmcnt(0)
	v_lshlrev_b32_e32 v176, 16, v240
	v_and_b32_e32 v177, 0xffff0000, v240
	v_lshlrev_b32_e32 v240, 16, v241
	v_and_b32_e32 v241, 0xffff0000, v241
	v_lshlrev_b32_e32 v178, 16, v242
	v_and_b32_e32 v179, 0xffff0000, v242
	v_lshlrev_b32_e32 v242, 16, v243
	v_and_b32_e32 v243, 0xffff0000, v243
	v_pk_add_f32 v[14:15], v[14:15], v[240:241]
	v_pk_add_f32 v[6:7], v[6:7], v[242:243]
	v_pk_add_f32 v[12:13], v[12:13], v[176:177]
	v_pk_add_f32 v[4:5], v[4:5], v[178:179]
	s_waitcnt vmcnt(0)
	v_lshlrev_b32_e32 v158, 16, v244
	v_and_b32_e32 v159, 0xffff0000, v244
	v_lshlrev_b32_e32 v244, 16, v245
	v_and_b32_e32 v245, 0xffff0000, v245
	v_lshlrev_b32_e32 v176, 16, v246
	v_and_b32_e32 v177, 0xffff0000, v246
	v_lshlrev_b32_e32 v246, 16, v247
	v_and_b32_e32 v247, 0xffff0000, v247
	v_pk_add_f32 v[10:11], v[10:11], v[244:245]
	v_pk_add_f32 v[8:9], v[8:9], v[158:159]
	v_pk_add_f32 v[2:3], v[2:3], v[246:247]
	v_pk_add_f32 v[0:1], v[0:1], v[176:177]

.LBB0_1291:
	v_subrev_co_u32_e32 v136, vcc, 1, v136
	s_and_b64 vcc, exec, vcc
	s_cbranch_vccnz .LBB0_1290
	s_ashr_i32 s29, s28, 31
	s_lshl_b64 s[48:49], s[28:29], 17
	v_lshl_add_u64 v[148:149], v[138:139], 0, s[48:49]
	global_load_dwordx4 v[184:187], v[148:149], off
	global_load_dwordx4 v[188:191], v[148:149], off offset:1024
	v_add_co_u32_e32 v248, vcc, 0x4000, v148
	s_nop 1
	v_addc_co_u32_e32 v249, vcc, 0, v149, vcc
	global_load_dwordx4 v[192:195], v[248:249], off
	global_load_dwordx4 v[196:199], v[248:249], off offset:1024
	v_add_co_u32_e32 v248, vcc, 0x8000, v148
	s_nop 1
	v_addc_co_u32_e32 v249, vcc, 0, v149, vcc
	global_load_dwordx4 v[200:203], v[248:249], off
	global_load_dwordx4 v[204:207], v[248:249], off offset:1024
	v_add_co_u32_e32 v248, vcc, 0xc000, v148
	s_nop 1
	v_addc_co_u32_e32 v249, vcc, 0, v149, vcc
	global_load_dwordx4 v[208:211], v[248:249], off
	global_load_dwordx4 v[212:215], v[248:249], off offset:1024
	v_add_co_u32_e32 v248, vcc, 0x10000, v148
	s_nop 1
	v_addc_co_u32_e32 v249, vcc, 0, v149, vcc
	global_load_dwordx4 v[216:219], v[248:249], off
	global_load_dwordx4 v[220:223], v[248:249], off offset:1024
	v_add_co_u32_e32 v248, vcc, 0x14000, v148
	s_nop 1
	v_addc_co_u32_e32 v249, vcc, 0, v149, vcc
	global_load_dwordx4 v[224:227], v[248:249], off
	global_load_dwordx4 v[228:231], v[248:249], off offset:1024
	v_add_co_u32_e32 v248, vcc, 0x18000, v148
	s_nop 1
	v_addc_co_u32_e32 v249, vcc, 0, v149, vcc
	global_load_dwordx4 v[232:235], v[248:249], off
	global_load_dwordx4 v[236:239], v[248:249], off offset:1024
	v_add_co_u32_e32 v248, vcc, 0x1c000, v148
	s_nop 1
	v_addc_co_u32_e32 v249, vcc, 0, v149, vcc
	global_load_dwordx4 v[240:243], v[248:249], off
	global_load_dwordx4 v[244:247], v[248:249], off offset:1024
	s_andn2_b64 vcc, exec, s[30:31]
	s_cbranch_vccnz .LBB0_1300
	s_waitcnt vmcnt(0)
	v_lshlrev_b32_e32 v162, 16, v184
	v_and_b32_e32 v163, 0xffff0000, v184
	v_lshlrev_b32_e32 v184, 16, v185
	v_and_b32_e32 v185, 0xffff0000, v185
	v_lshlrev_b32_e32 v164, 16, v186
	v_and_b32_e32 v165, 0xffff0000, v186
	v_lshlrev_b32_e32 v186, 16, v187
	v_and_b32_e32 v187, 0xffff0000, v187
	v_pk_add_f32 v[126:127], v[126:127], v[184:185]
	v_pk_add_f32 v[122:123], v[122:123], v[186:187]
	v_pk_add_f32 v[124:125], v[124:125], v[162:163]
	v_pk_add_f32 v[120:121], v[120:121], v[164:165]
	s_waitcnt vmcnt(0)
	v_lshlrev_b32_e32 v162, 16, v188
	v_and_b32_e32 v163, 0xffff0000, v188
	v_lshlrev_b32_e32 v188, 16, v189
	v_and_b32_e32 v189, 0xffff0000, v189
	v_lshlrev_b32_e32 v164, 16, v190
	v_and_b32_e32 v165, 0xffff0000, v190
	v_lshlrev_b32_e32 v190, 16, v191
	v_and_b32_e32 v191, 0xffff0000, v191
	v_pk_add_f32 v[114:115], v[114:115], v[188:189]
	v_pk_add_f32 v[112:113], v[112:113], v[162:163]
	v_pk_add_f32 v[106:107], v[106:107], v[190:191]
	v_pk_add_f32 v[104:105], v[104:105], v[164:165]
	s_andn2_b64 vcc, exec, s[36:37]
	s_cbranch_vccz .LBB0_1301

.LBB0_1295:
	s_waitcnt vmcnt(0)
	v_lshlrev_b32_e32 v164, 16, v200
	v_and_b32_e32 v165, 0xffff0000, v200
	v_lshlrev_b32_e32 v200, 16, v201
	v_and_b32_e32 v201, 0xffff0000, v201
	v_lshlrev_b32_e32 v166, 16, v202
	v_and_b32_e32 v167, 0xffff0000, v202
	v_lshlrev_b32_e32 v202, 16, v203
	v_and_b32_e32 v203, 0xffff0000, v203
	v_pk_add_f32 v[102:103], v[102:103], v[200:201]
	v_pk_add_f32 v[94:95], v[94:95], v[202:203]
	v_pk_add_f32 v[100:101], v[100:101], v[164:165]
	v_pk_add_f32 v[92:93], v[92:93], v[166:167]
	s_waitcnt vmcnt(0)
	v_lshlrev_b32_e32 v162, 16, v204
	v_and_b32_e32 v163, 0xffff0000, v204
	v_lshlrev_b32_e32 v204, 16, v205
	v_and_b32_e32 v205, 0xffff0000, v205
	v_lshlrev_b32_e32 v164, 16, v206
	v_and_b32_e32 v165, 0xffff0000, v206
	v_lshlrev_b32_e32 v206, 16, v207
	v_and_b32_e32 v207, 0xffff0000, v207
	v_pk_add_f32 v[82:83], v[82:83], v[204:205]
	v_pk_add_f32 v[80:81], v[80:81], v[162:163]
	v_pk_add_f32 v[74:75], v[74:75], v[206:207]
	v_pk_add_f32 v[72:73], v[72:73], v[164:165]
	s_andn2_b64 vcc, exec, s[40:41]
	s_cbranch_vccz .LBB0_1303

.LBB0_1297:
	s_waitcnt vmcnt(0)
	v_lshlrev_b32_e32 v164, 16, v216
	v_and_b32_e32 v165, 0xffff0000, v216
	v_lshlrev_b32_e32 v216, 16, v217
	v_and_b32_e32 v217, 0xffff0000, v217
	v_lshlrev_b32_e32 v166, 16, v218
	v_and_b32_e32 v167, 0xffff0000, v218
	v_lshlrev_b32_e32 v218, 16, v219
	v_and_b32_e32 v219, 0xffff0000, v219
	v_pk_add_f32 v[62:63], v[62:63], v[216:217]
	v_pk_add_f32 v[58:59], v[58:59], v[218:219]
	v_pk_add_f32 v[60:61], v[60:61], v[164:165]
	v_pk_add_f32 v[56:57], v[56:57], v[166:167]
	s_waitcnt vmcnt(0)
	v_lshlrev_b32_e32 v162, 16, v220
	v_and_b32_e32 v163, 0xffff0000, v220
	v_lshlrev_b32_e32 v220, 16, v221
	v_and_b32_e32 v221, 0xffff0000, v221
	v_lshlrev_b32_e32 v164, 16, v222
	v_and_b32_e32 v165, 0xffff0000, v222
	v_lshlrev_b32_e32 v222, 16, v223
	v_and_b32_e32 v223, 0xffff0000, v223
	v_pk_add_f32 v[50:51], v[50:51], v[220:221]
	v_pk_add_f32 v[48:49], v[48:49], v[162:163]
	v_pk_add_f32 v[42:43], v[42:43], v[222:223]
	v_pk_add_f32 v[40:41], v[40:41], v[164:165]
	s_andn2_b64 vcc, exec, s[44:45]
	s_cbranch_vccz .LBB0_1305

.LBB0_1299:
	s_waitcnt vmcnt(0)
	v_lshlrev_b32_e32 v164, 16, v232
	v_and_b32_e32 v165, 0xffff0000, v232
	v_lshlrev_b32_e32 v232, 16, v233
	v_and_b32_e32 v233, 0xffff0000, v233
	v_lshlrev_b32_e32 v166, 16, v234
	v_and_b32_e32 v167, 0xffff0000, v234
	v_lshlrev_b32_e32 v234, 16, v235
	v_and_b32_e32 v235, 0xffff0000, v235
	v_pk_add_f32 v[38:39], v[38:39], v[232:233]
	v_pk_add_f32 v[30:31], v[30:31], v[234:235]
	v_pk_add_f32 v[36:37], v[36:37], v[164:165]
	v_pk_add_f32 v[28:29], v[28:29], v[166:167]
	s_waitcnt vmcnt(0)
	v_lshlrev_b32_e32 v162, 16, v236
	v_and_b32_e32 v163, 0xffff0000, v236
	v_lshlrev_b32_e32 v236, 16, v237
	v_and_b32_e32 v237, 0xffff0000, v237
	v_lshlrev_b32_e32 v164, 16, v238
	v_and_b32_e32 v165, 0xffff0000, v238
	v_lshlrev_b32_e32 v238, 16, v239
	v_and_b32_e32 v239, 0xffff0000, v239
	v_pk_add_f32 v[18:19], v[18:19], v[236:237]
	v_pk_add_f32 v[16:17], v[16:17], v[162:163]
	v_pk_add_f32 v[10:11], v[10:11], v[238:239]
	v_pk_add_f32 v[8:9], v[8:9], v[164:165]
	s_andn2_b64 vcc, exec, s[62:63]
	s_cbranch_vccnz .LBB0_1290
	s_branch .LBB0_1307

.LBB0_1301:
	s_waitcnt vmcnt(0)
	v_lshlrev_b32_e32 v164, 16, v192
	v_and_b32_e32 v165, 0xffff0000, v192
	v_lshlrev_b32_e32 v192, 16, v193
	v_and_b32_e32 v193, 0xffff0000, v193
	v_lshlrev_b32_e32 v166, 16, v194
	v_and_b32_e32 v167, 0xffff0000, v194
	v_lshlrev_b32_e32 v194, 16, v195
	v_and_b32_e32 v195, 0xffff0000, v195
	v_pk_add_f32 v[118:119], v[118:119], v[192:193]
	v_pk_add_f32 v[110:111], v[110:111], v[194:195]
	v_pk_add_f32 v[116:117], v[116:117], v[164:165]
	v_pk_add_f32 v[108:109], v[108:109], v[166:167]
	s_waitcnt vmcnt(0)
	v_lshlrev_b32_e32 v162, 16, v196
	v_and_b32_e32 v163, 0xffff0000, v196
	v_lshlrev_b32_e32 v196, 16, v197
	v_and_b32_e32 v197, 0xffff0000, v197
	v_lshlrev_b32_e32 v164, 16, v198
	v_and_b32_e32 v165, 0xffff0000, v198
	v_lshlrev_b32_e32 v198, 16, v199
	v_and_b32_e32 v199, 0xffff0000, v199
	v_pk_add_f32 v[98:99], v[98:99], v[196:197]
	v_pk_add_f32 v[96:97], v[96:97], v[162:163]
	v_pk_add_f32 v[90:91], v[90:91], v[198:199]
	v_pk_add_f32 v[88:89], v[88:89], v[164:165]
	s_andn2_b64 vcc, exec, s[38:39]
	s_cbranch_vccz .LBB0_1295

.LBB0_1303:
	s_waitcnt vmcnt(0)
	v_lshlrev_b32_e32 v164, 16, v208
	v_and_b32_e32 v165, 0xffff0000, v208
	v_lshlrev_b32_e32 v208, 16, v209
	v_and_b32_e32 v209, 0xffff0000, v209
	v_lshlrev_b32_e32 v166, 16, v210
	v_and_b32_e32 v167, 0xffff0000, v210
	v_lshlrev_b32_e32 v210, 16, v211
	v_and_b32_e32 v211, 0xffff0000, v211
	v_pk_add_f32 v[86:87], v[86:87], v[208:209]
	v_pk_add_f32 v[78:79], v[78:79], v[210:211]
	v_pk_add_f32 v[84:85], v[84:85], v[164:165]
	v_pk_add_f32 v[76:77], v[76:77], v[166:167]
	s_waitcnt vmcnt(0)
	v_lshlrev_b32_e32 v162, 16, v212
	v_and_b32_e32 v163, 0xffff0000, v212
	v_lshlrev_b32_e32 v212, 16, v213
	v_and_b32_e32 v213, 0xffff0000, v213
	v_lshlrev_b32_e32 v164, 16, v214
	v_and_b32_e32 v165, 0xffff0000, v214
	v_lshlrev_b32_e32 v214, 16, v215
	v_and_b32_e32 v215, 0xffff0000, v215
	v_pk_add_f32 v[70:71], v[70:71], v[212:213]
	v_pk_add_f32 v[68:69], v[68:69], v[162:163]
	v_pk_add_f32 v[66:67], v[66:67], v[214:215]
	v_pk_add_f32 v[64:65], v[64:65], v[164:165]
	s_andn2_b64 vcc, exec, s[42:43]
	s_cbranch_vccz .LBB0_1297

.LBB0_1305:
	s_waitcnt vmcnt(0)
	v_lshlrev_b32_e32 v164, 16, v224
	v_and_b32_e32 v165, 0xffff0000, v224
	v_lshlrev_b32_e32 v224, 16, v225
	v_and_b32_e32 v225, 0xffff0000, v225
	v_lshlrev_b32_e32 v166, 16, v226
	v_and_b32_e32 v167, 0xffff0000, v226
	v_lshlrev_b32_e32 v226, 16, v227
	v_and_b32_e32 v227, 0xffff0000, v227
	v_pk_add_f32 v[54:55], v[54:55], v[224:225]
	v_pk_add_f32 v[46:47], v[46:47], v[226:227]
	v_pk_add_f32 v[52:53], v[52:53], v[164:165]
	v_pk_add_f32 v[44:45], v[44:45], v[166:167]
	s_waitcnt vmcnt(0)
	v_lshlrev_b32_e32 v162, 16, v228
	v_and_b32_e32 v163, 0xffff0000, v228
	v_lshlrev_b32_e32 v228, 16, v229
	v_and_b32_e32 v229, 0xffff0000, v229
	v_lshlrev_b32_e32 v164, 16, v230
	v_and_b32_e32 v165, 0xffff0000, v230
	v_lshlrev_b32_e32 v230, 16, v231
	v_and_b32_e32 v231, 0xffff0000, v231
	v_pk_add_f32 v[34:35], v[34:35], v[228:229]
	v_pk_add_f32 v[32:33], v[32:33], v[162:163]
	v_pk_add_f32 v[26:27], v[26:27], v[230:231]
	v_pk_add_f32 v[24:25], v[24:25], v[164:165]
	s_andn2_b64 vcc, exec, s[46:47]
	s_cbranch_vccz .LBB0_1299

.LBB0_1307:
	s_waitcnt vmcnt(0)
	v_lshlrev_b32_e32 v162, 16, v240
	v_and_b32_e32 v163, 0xffff0000, v240
	v_lshlrev_b32_e32 v240, 16, v241
	v_and_b32_e32 v241, 0xffff0000, v241
	v_lshlrev_b32_e32 v164, 16, v242
	v_and_b32_e32 v165, 0xffff0000, v242
	v_lshlrev_b32_e32 v242, 16, v243
	v_and_b32_e32 v243, 0xffff0000, v243
	v_pk_add_f32 v[22:23], v[22:23], v[240:241]
	v_pk_add_f32 v[14:15], v[14:15], v[242:243]
	v_pk_add_f32 v[20:21], v[20:21], v[162:163]
	v_pk_add_f32 v[12:13], v[12:13], v[164:165]
	s_waitcnt vmcnt(0)
	v_lshlrev_b32_e32 v148, 16, v244
	v_and_b32_e32 v149, 0xffff0000, v244
	v_lshlrev_b32_e32 v244, 16, v245
	v_and_b32_e32 v245, 0xffff0000, v245
	v_lshlrev_b32_e32 v162, 16, v246
	v_and_b32_e32 v163, 0xffff0000, v246
	v_lshlrev_b32_e32 v246, 16, v247
	v_and_b32_e32 v247, 0xffff0000, v247
	v_pk_add_f32 v[6:7], v[6:7], v[244:245]
	v_pk_add_f32 v[4:5], v[4:5], v[148:149]
	v_pk_add_f32 v[2:3], v[2:3], v[246:247]
	v_pk_add_f32 v[0:1], v[0:1], v[162:163]
	s_branch .LBB0_1290
